# Fourier stage A unit loop: the wait before staging the prefetched tile counts only what is older than the previous unit's eight output stores (vmcnt 8 instead of 0), so store acknowledgements are no l
# speedup vs baseline: 1.0076x; 1.0076x over previous
; #define LAS __attribute__((address_space(3)))
;     __device__ __forceinline__ bf16_t* dft() const { return (bf16_t*)(ws + WS_DFT); }
; #define FA_LOAD(u) do { const int _b = (u) >> 8, _n2 = ((u) >> 2) & 63, _cb = (u) & 3; \
;         _Pragma("unroll") for (int _q = 0; _q < 4; ++_q) { const int _n1 = (_q >> 1) * 64 + (_q & 1) * 32 + sr; \
;             pf[_q] = *(const bf16x8*)(F.proj() + (size_t)(_b * SEQ + 64 * _n1 + _n2) * INW + C_FX + _cb * 128 + sc); } } while (0)
; __device__ __forceinline__ void phase_fft_a(const Frame& F) {
;     const int tid = F.tid, wid = F.wid, lane = F.lane, r32 = lane & 31, hi = lane >> 5;
;     LAS char* Vt = (LAS char*)F.lds;
;     const int sr = tid >> 4, sc = (tid & 15) * 8;
;     const int rb = wid & 3, chh = wid >> 2, k1 = 32 * rb + r32;
;     const bf16_t* dc = F.dft(); const bf16_t* ds = F.dft() + 16384;
;     const int NU = NB * 64 * 4;
;     bf16x8 pf[4];
;     ...
;     int u = F.wg, par = 0;
;     if (u < NU) FA_LOAD(u);
.LBB0_324:
	s_or_b64 exec, exec, s[44:45]
	v_readlane_b32 s8, v252, 54
	v_mov_b32_e32 v2, v0
	v_readlane_b32 s9, v252, 55
	s_andn2_b64 vcc, exec, s[8:9]
	v_readfirstlane_b32 s0, v2
	v_readlane_b32 s31, v254, 5
	s_cbranch_vccnz .LBB0_331
	s_lshr_b32 s1, s0, 1
	v_ashrrev_i32_e32 v5, 4, v2
	s_and_b32 s1, s1, 0x60
	v_lshlrev_b32_e32 v1, 6, v5
	v_readlane_b32 s2, v252, 56
	s_add_u32 s8, s56, 0xc8000
	s_addc_u32 s9, s57, 0
	v_add_u32_e32 v6, s2, v1
	v_ashrrev_i32_e32 v7, 31, v6
	s_add_u32 s18, s56, 0xc0000
	v_lshlrev_b32_e32 v3, 3, v2
	v_lshlrev_b64 v[8:9], 13, v[6:7]
	v_readlane_b32 s2, v252, 57
	v_add_u32_e32 v10, 0x800, v6
	s_addc_u32 s19, s57, 0
	v_and_b32_e32 v4, 0x78, v3
	v_lshl_add_u64 v[8:9], s[56:57], 0, v[8:9]
	s_lshl_b32 s76, s2, 1
	v_ashrrev_i32_e32 v11, 31, v10
	v_lshl_add_u64 v[8:9], v[8:9], 0, s[76:77]
	v_lshlrev_b32_e32 v146, 1, v4
	v_lshlrev_b64 v[10:11], 13, v[10:11]
	v_lshl_add_u64 v[8:9], v[8:9], 0, v[146:147]
	s_mov_b32 s2, 0x1c317000
	v_lshl_add_u64 v[10:11], s[56:57], 0, v[10:11]
	v_add_co_u32_e32 v8, vcc, s2, v8
	v_lshl_add_u64 v[10:11], v[10:11], 0, s[76:77]
	s_nop 0
	v_addc_co_u32_e32 v9, vcc, 0, v9, vcc
	v_lshl_add_u64 v[10:11], v[10:11], 0, v[146:147]
	v_add_co_u32_e32 v10, vcc, s2, v10
	v_and_or_b32 v120, v2, 31, s1
	s_nop 0
	v_addc_co_u32_e32 v11, vcc, 0, v11, vcc
	global_load_dwordx4 v[66:69], v[8:9], off offset:2304
	global_load_dwordx4 v[70:73], v[10:11], off offset:2304
	v_add_u32_e32 v8, 0x1000, v6
	v_ashrrev_i32_e32 v9, 31, v8
	v_lshlrev_b64 v[8:9], 13, v[8:9]
	v_add_u32_e32 v6, 0x1800, v6
	v_lshl_add_u64 v[8:9], s[56:57], 0, v[8:9]
	v_ashrrev_i32_e32 v7, 31, v6
	v_lshl_add_u64 v[8:9], v[8:9], 0, s[76:77]
	v_lshlrev_b64 v[6:7], 13, v[6:7]
	v_lshl_add_u64 v[8:9], v[8:9], 0, v[146:147]
	v_lshl_add_u64 v[6:7], s[56:57], 0, v[6:7]
	v_add_co_u32_e32 v8, vcc, s2, v8
	v_lshl_add_u64 v[6:7], v[6:7], 0, s[76:77]
	s_nop 0
	v_addc_co_u32_e32 v9, vcc, 0, v9, vcc
	v_lshl_add_u64 v[6:7], v[6:7], 0, v[146:147]
	v_add_co_u32_e32 v6, vcc, s2, v6
	s_ashr_i32 s1, s0, 8
	s_nop 0
	v_addc_co_u32_e32 v7, vcc, 0, v7, vcc
	global_load_dwordx4 v[74:77], v[8:9], off offset:2304
	global_load_dwordx4 v[78:81], v[6:7], off offset:2304
	v_lshrrev_b32_e32 v7, 1, v5
	v_and_b32_e32 v9, 3, v5
	v_and_or_b32 v7, v7, 4, v9
	v_lshlrev_b32_e32 v121, 6, v7
	v_lshlrev_b32_e32 v7, 4, v2
	v_bfe_u32 v6, v2, 5, 1
	v_and_b32_e32 v122, 48, v7
	v_and_b32_e32 v7, 0xc0, v7
	v_lshlrev_b32_e32 v2, 1, v2
	v_bfe_u32 v8, v3, 5, 2
	v_and_b32_e32 v2, 32, v2
	v_lshl_or_b32 v7, s1, 10, v7
	v_and_b32_e32 v3, 0x118, v3
	v_or3_b32 v123, v7, v3, v2
	v_and_b32_e32 v3, 0xfffff0, v5
	v_lshlrev_b32_e32 v7, 1, v5
	v_and_or_b32 v3, v7, 8, v3
	v_lshrrev_b32_e32 v3, 1, v3
	v_or_b32_e32 v3, v3, v8
	v_lshlrev_b32_e32 v124, 9, v3
	v_add_u32_e32 v3, 32, v5
	v_and_b32_e32 v5, 0xfffff0, v3
	v_lshlrev_b32_e32 v3, 1, v3
	v_and_or_b32 v3, v3, 8, v5
	v_lshrrev_b32_e32 v3, 1, v3
	v_or_b32_e32 v3, v3, v8
	v_lshlrev_b32_e32 v125, 9, v3
	v_lshlrev_b32_e32 v3, 8, v120
	v_lshl_or_b32 v146, v6, 4, v3
	v_lshlrev_b32_e32 v2, 2, v6
	v_or_b32_e32 v6, 32, v146
	v_mov_b32_e32 v7, v147
	v_lshl_add_u64 v[86:87], s[18:19], 0, v[6:7]
	v_lshl_add_u64 v[88:89], s[8:9], 0, v[6:7]
	v_or_b32_e32 v6, 64, v146
	s_lshl_b32 s28, s1, 6
	v_lshl_add_u64 v[90:91], s[18:19], 0, v[6:7]
	v_lshl_add_u64 v[92:93], s[8:9], 0, v[6:7]
	v_or_b32_e32 v6, 0x60, v146
	s_ashr_i32 s29, s28, 31
	v_lshl_add_u64 v[94:95], s[18:19], 0, v[6:7]
	v_lshl_add_u64 v[96:97], s[8:9], 0, v[6:7]
	v_or_b32_e32 v6, 0x80, v146
	v_lshl_add_u64 v[98:99], s[18:19], 0, v[6:7]
	v_lshl_add_u64 v[100:101], s[8:9], 0, v[6:7]
	v_or_b32_e32 v6, 0xa0, v146
	s_add_u32 s40, s56, 0xb0000
	v_lshl_add_u64 v[82:83], s[18:19], 0, v[146:147]
	v_lshl_add_u64 v[84:85], s[8:9], 0, v[146:147]
	v_lshl_add_u64 v[102:103], s[18:19], 0, v[6:7]
	v_lshl_add_u64 v[104:105], s[8:9], 0, v[6:7]
	v_or_b32_e32 v6, 0xc0, v146
	v_or_b32_e32 v146, 0xe0, v146
	s_addc_u32 s41, s57, 0
	v_lshlrev_b32_e32 v9, 7, v120
	v_lshl_add_u64 v[108:109], s[8:9], 0, v[6:7]
	v_lshl_add_u64 v[112:113], s[8:9], 0, v[146:147]
	s_add_u32 s24, s56, 0x3d316100
	v_readlane_b32 s8, v254, 62
	s_mov_b32 s0, 0
	v_lshl_add_u64 v[106:107], s[18:19], 0, v[6:7]
	v_lshl_add_u64 v[110:111], s[18:19], 0, v[146:147]
	s_addc_u32 s25, s57, 0
	v_lshlrev_b32_e32 v114, 1, v4
	v_lshlrev_b32_e32 v126, 2, v9
	v_lshlrev_b32_e32 v146, 1, v2
	v_readlane_b32 s1, v253, 60
	v_readlane_b32 s22, v253, 15
	s_mov_b32 s23, s8
	v_readlane_b32 s9, v254, 63
	v_and_b32_e32 v176, 31, v0
	v_mul_u32_u24_e32 v176, 0x110, v176
	v_bfe_u32 v177, v0, 5, 1
	v_lshl_add_u32 v176, v177, 3, v176
	v_lshrrev_b32_e32 v177, 6, v0
	v_mul_u32_u24_e32 v177, 0x2200, v177
	v_add_u32_e32 v177, 0x10000, v177
	v_add_u32_e32 v176, v176, v177
	v_bfe_u32 v178, v0, 3, 3
	v_mul_u32_u24_e32 v178, 0x110, v178
	v_add_u32_e32 v177, v177, v178
	v_and_b32_e32 v178, 7, v0
	v_lshl_add_u32 v177, v178, 4, v177
	v_bfe_u32 v120, v0, 3, 3
	v_bfe_u32 v178, v0, 6, 2
	v_lshl_or_b32 v120, v178, 5, v120
	v_and_b32_e32 v146, 7, v0
	v_lshlrev_b32_e32 v146, 4, v146
	s_waitcnt vmcnt(0)
	s_branch .LBB0_327

; #define LAS __attribute__((address_space(3)))
; __device__ __forceinline__ int v_st(int k, int c) { const int kk = (k & ~0xC) | ((k & 4) << 1) | ((k & 8) >> 1); return ((kk >> 3) * 4 + (c >> 5)) * 512 + ((kk & 7) * 32 + (c & 31)) * 2; }
; __device__ __forceinline__ void phase_fft_a(const Frame& F) {
;     ...
;     for (; u < NU; u += F.nwg, par ^= 1) {
;         const int b = u >> 8, n2 = (u >> 2) & 63, cb = u & 3;
;         LAS char* img = Vt + par * 32768;
; #pragma unroll
;         for (int q = 0; q < 4; ++q) *(LAS bf16x8*)(img + (q >> 1) * 16384 + ff::v_st((q & 1) * 32 + sr, sc)) = pf[q];
;         __syncthreads();
.LBB0_327:
	s_lshl_b32 s2, s0, 15
	s_add_i32 s30, s2, 0
	s_add_i32 s2, s23, s96
	v_add_u32_e32 v2, s30, v124
	v_add_u32_e32 v3, s30, v125
	s_cmpk_gt_i32 s2, 0x7ff
	v_add3_u32 v2, v2, v121, v122
	v_add3_u32 v3, v3, v121, v122
	s_cselect_b64 s[18:19], -1, 0
	s_cmpk_lt_i32 s2, 0x800
	s_mov_b64 s[8:9], -1
	s_waitcnt vmcnt(8)
	ds_write_b128 v2, v[66:69]
	ds_write_b128 v3, v[70:73]
	ds_write_b128 v2, v[74:77] offset:16384
	ds_write_b128 v3, v[78:81] offset:16384
	s_waitcnt lgkmcnt(0)
	s_barrier
	s_cbranch_scc1 .LBB0_329
	v_readlane_b32 s7, v254, 4
	s_add_i32 s7, s22, s7
	s_mov_b64 s[8:9], 0
